# P0 role split retuned: 7 helper CUs per XCD (56) convert x rows [0,12288); 200 CUs stream transposes
# baseline (speedup 1.0000x reference)
.LBB0_14:
	s_mov_b32 s99, s43
	s_mov_b32 s98, s42
	s_cmp_lg_u32 s42, 0x100
	s_cbranch_scc1 .Lp0_go
	s_and_b32 s98, s43, 31
	s_lshr_b32 s99, s43, 5
	s_cmp_lt_u32 s98, 7
	s_cbranch_scc1 .Lp0_roleB
	s_mul_i32 s99, s99, 25
	s_add_i32 s99, s99, s98
	s_add_i32 s99, s99, -7
	s_movk_i32 s98, 0xc8
	s_branch .Lp0_go
.Lp0_roleB:
	s_movk_i32 s99, 0x4000
	s_movk_i32 s98, 0xc8

.LBB0_898:
	s_lshl_b32 s8, s43, 3
	s_add_i32 s8, s8, s91
	s_lshl_b32 s10, s42, 3
	s_movk_i32 s99, 0x3fff
	s_cmp_lg_u32 s42, 0x100
	s_cbranch_scc1 .Lp0_xs_done
	s_and_b32 s98, s43, 31
	s_lshr_b32 s8, s43, 5
	s_cmp_lt_u32 s98, 7
	s_cbranch_scc1 .Lp0_xs_B
	s_mul_i32 s8, s8, 25
	s_add_i32 s8, s8, s98
	s_add_i32 s8, s8, -7
	s_lshl_b32 s8, s8, 3
	s_add_i32 s8, s8, s91
	s_addk_i32 s8, 0x3000
	s_movk_i32 s10, 0x640
	s_branch .Lp0_xs_done
.Lp0_xs_B:
	s_mul_i32 s8, s8, 7
	s_add_i32 s8, s8, s98
	s_lshl_b32 s8, s8, 3
	s_add_i32 s8, s8, s91
	s_movk_i32 s10, 0x1c0
	s_movk_i32 s99, 0x2fff

.LBB0_913:
	s_cmp_lg_u32 s42, 0x100
	s_cbranch_scc1 .Lp0_noremap
	s_and_b32 s98, s43, 31
	s_lshr_b32 s99, s43, 5
	s_cmp_lt_u32 s98, 7
	s_cbranch_scc1 .Lp0_foldB
	s_movk_i32 s43, 0x100
	s_branch .Lp0_foldset
.Lp0_foldB:
	s_mul_i32 s99, s99, 7
	s_add_i32 s43, s99, s98
.Lp0_foldset:
	s_movk_i32 s42, 56
	s_lshl_b32 s22, s43, 9
	s_lshl_b32 s0, s42, 9
